# stack5 + the two compiler vmcnt(0) drains right after the first K/V tile DMAs of every attention unit relaxed to counted waits (diff vmcnt(1), SWA vmcnt(4))
# speedup vs baseline: 1.0134x; 1.0027x over previous
; #define LAS __attribute__((address_space(3)))
; template <bool HAVE_PREV, bool HAVE_NEXT> __device__ __forceinline__ void dstep(f32x16& ca, f32x16& cb, f32x16& pa, f32x16& pb, const bf16x8 (&kf)[4], bf16x8 (&kn)[4], const LAS unsigned char* kbn, unsigned vpa, ...
;     const f32x16 z = {0.f, 0.f, 0.f, 0.f, 0.f, 0.f, 0.f, 0.f, 0.f, 0.f, 0.f, 0.f, 0.f, 0.f, 0.f, 0.f};
;     s16x4 vl[2][2], vh[2][2]; u32x4 wa[2], wb[2];
;     ca = __builtin_amdgcn_mfma_f32_32x32x16_bf16(kf[0], qr[0], z, 0, 0, 0);
;     float a0, a1, a2, a3, a4, a5, a6, a7, b0, b1, b2, b3, b4, b5, b6, b7;
;     if (HAVE_PREV) { a0 = fadd_s(pa[0], pa[1]); a1 = fadd_s(pa[2], pa[3]); a2 = fadd_s(pa[4], pa[5]); a3 = fadd_s(pa[6], pa[7]); a4 = fadd_s(pa[8], pa[9]); a5 = fadd_s(pa[10], pa[11]); a6 = fadd_s(pa[12], pa[13]); a7 = fadd_s(pa[14], pa[15]);
;         wa[0].x = cvtpk(pa[0], pa[1]); wa[0].y = cvtpk(pa[2], pa[3]); wa[0].z = cvtpk(pa[4], pa[5]); wa[0].w = cvtpk(pa[6], pa[7]); }
;     ATT_SB();
;     ca = __builtin_amdgcn_mfma_f32_32x32x16_bf16(kf[1], qr[1], ca, 0, 0, 0);
;     if (HAVE_PREV) {
;         ATT_TR(vl[0][0], vpa, 0); ATT_TR(vh[0][0], vpa, 512); ATT_TR(vl[1][0], vpa, 4096); ATT_TR(vh[1][0], vpa, 4096 + 512);
;         ATT_TR(vl[0][1], vpa, 1024); ATT_TR(vh[0][1], vpa, 1024 + 512); ATT_TR(vl[1][1], vpa, 4096 + 1024); ATT_TR(vh[1][1], vpa, 4096 + 1024 + 512);
;         a0 = fadd_s(a0, a1); a2 = fadd_s(a2, a3); a4 = fadd_s(a4, a5); a6 = fadd_s(a6, a7);
;         wa[1].x = cvtpk(pa[8], pa[9]); wa[1].y = cvtpk(pa[10], pa[11]); wa[1].z = cvtpk(pa[12], pa[13]); wa[1].w = cvtpk(pa[14], pa[15]);
;         a0 = fadd_s(a0, a2); a4 = fadd_s(a4, a6); }
;     ATT_SB();
; __device__ __forceinline__ void unit_diff(const P& p, LAS unsigned char* lds, const Src& S, float lam, bf16_t* orow, const int wid,
;                                           bf16x8 (&qr)[4], const bool pre  , const bool pn  , const Src& Sn) {
;     ...
;     const unsigned lbase = (unsigned)(__SIZE_TYPE__)lds;
;     f32x16 A0, B0, A1, B1; bf16x8 kA[4], kB[4];
;     ATT_WAITV(0); ATT_BAR(); ATT_DMA(2, 2 * SLOTB); ATT_DMA(3, 3 * SLOTB);
; #pragma unroll
;     for (int d0 = 0; d0 < 4; ++d0) kA[d0] = *(const LAS bf16x8*)(lds + koff + d0 * 2048);
;     dstep<false, true>(A0, B0, A1, B1, kA, kB, lds + koff + 512, 0u, qr, o1, o2, l1, l2);
;     dstep<true, true>(A1, B1, A0, B0, kB, kA, lds + SLOTB + koff, lbase + voff, qr, o1, o2, l1, l2);
.LBB7_437:
	s_and_b32 s2, s58, 7
	s_lshl_b32 s10, s2, 13
	s_add_u32 s13, s79, s10
	s_addc_u32 s36, s80, 0
	s_add_u32 s10, s13, 0x8000
	s_addc_u32 s11, s36, 0
	v_lshlrev_b64 v[160:161], 1, v[0:1]
	s_add_u32 s13, s13, 0x18000
	s_waitcnt vmcnt(0)
	v_lshl_add_u64 v[0:1], s[56:57], 0, v[160:161]
	s_addc_u32 s36, s36, 0
	s_waitcnt lgkmcnt(0)
	s_barrier
	v_lshl_add_u64 v[2:3], v[0:1], 0, s[48:49]
	s_add_i32 m0, s96, 0x8000
	v_lshl_add_u64 v[0:1], v[0:1], 0, s[50:51]
	global_load_lds_dwordx4 v[2:3], off
	v_lshl_add_u64 v[2:3], s[54:55], 0, v[160:161]
	s_waitcnt vmcnt(1)
	v_lshl_add_u64 v[4:5], v[2:3], 0, s[48:49]
	s_mov_b32 m0, s42
	v_lshlrev_b32_e32 v49, 8, v170
	global_load_lds_dwordx4 v[4:5], off
	s_add_i32 m0, s96, 0xc000
	v_lshlrev_b32_e32 v4, 4, v169
	global_load_lds_dwordx4 v[0:1], off
	v_lshl_add_u64 v[0:1], v[2:3], 0, s[50:51]
	s_mov_b32 m0, s43
	v_lshlrev_b32_e32 v2, 3, v169
	global_load_lds_dwordx4 v[0:1], off
	v_lshlrev_b32_e32 v0, 4, v171
	v_lshl_or_b32 v0, v170, 10, v0
	v_lshlrev_b32_e32 v1, 1, v169
	v_and_b32_e32 v1, 32, v1
	v_add_u32_e32 v173, 0, v0
	v_and_or_b32 v48, v2, 24, v1
	ds_read_b128 v[0:3], v173
	s_waitcnt lgkmcnt(0)
	v_mfma_f32_32x32x16_bf16 v[16:31], v[0:3], v[128:131], 0
	v_and_b32_e32 v50, 0xc0, v4
	ds_read_b128 v[4:7], v173 offset:2048
	ds_read_b128 v[8:11], v173 offset:4096
	ds_read_b128 v[32:35], v173 offset:6144
	s_mov_b32 s59, 0x8000
	s_mov_b32 s37, 0xc000
	s_waitcnt lgkmcnt(0)
	v_mfma_f32_32x32x16_bf16 v[16:31], v[4:7], v[132:135], v[16:31]
	v_mfma_f32_32x32x16_bf16 v[0:15], v[8:11], v[136:139], 0
	v_mfma_f32_32x32x16_bf16 v[0:15], v[32:35], v[140:143], v[0:15]
	s_waitcnt lgkmcnt(0)
	ds_read_b128 v[36:39], v173 offset:512
	ds_read_b128 v[40:43], v173 offset:2560
	ds_read_b128 v[44:47], v173 offset:4608
	ds_read_b128 v[32:35], v173 offset:6656
	s_nop 5
	v_exp_f32_e32 v16, v16
	v_exp_f32_e32 v17, v17
	v_exp_f32_e32 v18, v18
	v_exp_f32_e32 v19, v19
	s_nop 0
	v_exp_f32_e32 v20, v20
	v_exp_f32_e32 v21, v21
	v_exp_f32_e32 v22, v22
	v_exp_f32_e32 v23, v23
	s_nop 0
	v_exp_f32_e32 v24, v24
	v_exp_f32_e32 v25, v25
	v_exp_f32_e32 v26, v26
	v_exp_f32_e32 v27, v27
	s_nop 0
	v_exp_f32_e32 v28, v28
	v_exp_f32_e32 v29, v29
	v_exp_f32_e32 v30, v30
	v_exp_f32_e32 v31, v31
	v_exp_f32_e32 v0, v0
	v_exp_f32_e32 v1, v1
	v_exp_f32_e32 v2, v2
	v_exp_f32_e32 v3, v3
	s_nop 0
	v_exp_f32_e32 v4, v4
	v_exp_f32_e32 v5, v5
	v_exp_f32_e32 v6, v6
	v_exp_f32_e32 v7, v7
	s_nop 0
	v_exp_f32_e32 v8, v8
	v_exp_f32_e32 v9, v9
	v_exp_f32_e32 v10, v10
	v_exp_f32_e32 v11, v11
	s_nop 0
	v_exp_f32_e32 v12, v12
	v_exp_f32_e32 v13, v13
	v_exp_f32_e32 v14, v14
	v_exp_f32_e32 v15, v15
	s_waitcnt lgkmcnt(0)
	v_mfma_f32_32x32x16_bf16 v[80:95], v[36:39], v[128:131], 0
	s_add_i32 s53, 0, 0x2000
	v_add_u32_e32 v50, s53, v50
	v_add3_u32 v172, v50, v49, v48
	v_add_f32_e32 v52, v16, v17
	v_add_f32_e32 v53, v18, v19
	v_add_f32_e32 v54, v20, v21
	v_add_f32_e32 v55, v22, v23
	v_add_f32_e32 v56, v24, v25
	v_add_f32_e32 v57, v26, v27
	v_add_f32_e32 v58, v28, v29
	v_add_f32_e32 v59, v30, v31
	v_cvt_pk_bf16_f32 v16, v16, v17
	v_cvt_pk_bf16_f32 v17, v18, v19
	v_cvt_pk_bf16_f32 v18, v20, v21
	v_cvt_pk_bf16_f32 v19, v22, v23
	ds_read_b64_tr_b16 v[36:37], v172 offset:0
	ds_read_b64_tr_b16 v[38:39], v172 offset:512
	ds_read_b64_tr_b16 v[48:49], v172 offset:4096
	v_mfma_f32_32x32x16_bf16 v[80:95], v[40:43], v[132:135], v[80:95]
	ds_read_b64_tr_b16 v[50:51], v172 offset:4608
	ds_read_b64_tr_b16 v[104:105], v172 offset:1024
	ds_read_b64_tr_b16 v[106:107], v172 offset:1536
	ds_read_b64_tr_b16 v[100:101], v172 offset:5120
	ds_read_b64_tr_b16 v[102:103], v172 offset:5632
	v_add_f32_e32 v20, v52, v53
	v_add_f32_e32 v21, v54, v55
	v_add_f32_e32 v22, v56, v57
	v_add_f32_e32 v23, v58, v59
	v_cvt_pk_bf16_f32 v108, v24, v25
	v_cvt_pk_bf16_f32 v109, v26, v27
	v_cvt_pk_bf16_f32 v110, v28, v29
	v_cvt_pk_bf16_f32 v111, v30, v31
	s_nop 0
	v_add_f32_e32 v20, v20, v21
	v_add_f32_e32 v21, v22, v23
	v_mfma_f32_32x32x16_bf16 v[64:79], v[44:47], v[136:139], 0
	v_add_f32_e32 v22, v0, v1
	v_add_f32_e32 v23, v2, v3
	v_add_f32_e32 v24, v4, v5
	v_add_f32_e32 v25, v6, v7
	v_add_f32_e32 v26, v8, v9
	v_add_f32_e32 v27, v10, v11
	v_add_f32_e32 v28, v12, v13
	v_add_f32_e32 v29, v14, v15
	v_cvt_pk_bf16_f32 v52, v0, v1
	v_cvt_pk_bf16_f32 v53, v2, v3
	v_cvt_pk_bf16_f32 v54, v4, v5
	v_cvt_pk_bf16_f32 v55, v6, v7
	v_add_f32_e32 v0, v20, v21
	v_mfma_f32_32x32x16_bf16 v[64:79], v[32:35], v[140:143], v[64:79]
	v_add_f32_e32 v1, v22, v23
	v_add_f32_e32 v2, v24, v25
	v_add_f32_e32 v3, v26, v27
	v_add_f32_e32 v4, v28, v29
	v_cvt_pk_bf16_f32 v112, v8, v9
	v_cvt_pk_bf16_f32 v113, v10, v11
	v_cvt_pk_bf16_f32 v114, v12, v13
	v_cvt_pk_bf16_f32 v115, v14, v15
	s_nop 0
	v_add_f32_e32 v1, v1, v2
	v_add_f32_e32 v2, v3, v4
	v_add_f32_e32 v174, v166, v0
	s_mov_b32 s60, 0
	v_add_f32_e32 v0, v1, v2
	s_waitcnt lgkmcnt(0)
	s_nop 0
	v_add_f32_e32 v175, v166, v0
	v_mfma_f32_32x32x16_bf16 v[0:15], v[16:19], v[36:39], 0
	ds_read_b128 v[96:99], v173 offset:16384
	ds_read_b128 v[152:155], v173 offset:18432
	ds_read_b128 v[148:151], v173 offset:20480
	ds_read_b128 v[144:147], v173 offset:22528
	s_nop 0
	v_exp_f32_e32 v80, v80
	v_exp_f32_e32 v81, v81
	v_exp_f32_e32 v82, v82
	v_exp_f32_e32 v83, v83
	v_mfma_f32_32x32x16_bf16 v[16:31], v[16:19], v[48:51], 0
	v_exp_f32_e32 v84, v84
	v_exp_f32_e32 v85, v85
	v_exp_f32_e32 v86, v86
	v_exp_f32_e32 v87, v87
	v_mfma_f32_32x32x16_bf16 v[32:47], v[52:55], v[36:39], 0
	v_exp_f32_e32 v88, v88
	v_exp_f32_e32 v89, v89
	v_exp_f32_e32 v90, v90
	v_exp_f32_e32 v91, v91
	v_mfma_f32_32x32x16_bf16 v[48:63], v[52:55], v[48:51], 0
	v_exp_f32_e32 v92, v92
	v_exp_f32_e32 v93, v93
	v_exp_f32_e32 v94, v94
	v_exp_f32_e32 v95, v95
	v_mfma_f32_32x32x16_bf16 v[0:15], v[108:111], v[104:107], v[0:15]
	v_exp_f32_e32 v64, v64
	v_exp_f32_e32 v65, v65
	v_exp_f32_e32 v66, v66
	v_exp_f32_e32 v67, v67
	v_mfma_f32_32x32x16_bf16 v[16:31], v[108:111], v[100:103], v[16:31]
	v_exp_f32_e32 v68, v68
	v_exp_f32_e32 v69, v69
	v_exp_f32_e32 v70, v70
	v_exp_f32_e32 v71, v71
	v_mfma_f32_32x32x16_bf16 v[32:47], v[112:115], v[104:107], v[32:47]
	v_exp_f32_e32 v72, v72
	v_exp_f32_e32 v73, v73
	v_exp_f32_e32 v74, v74
	v_exp_f32_e32 v75, v75
	v_mfma_f32_32x32x16_bf16 v[48:63], v[112:115], v[100:103], v[48:63]
	v_exp_f32_e32 v76, v76
	v_exp_f32_e32 v77, v77
	v_exp_f32_e32 v78, v78
	v_exp_f32_e32 v79, v79
	s_add_u32 s54, s30, s0
	v_add_u32_e32 v176, 0x800, v172
	s_addc_u32 s55, s31, s1
	s_mov_b32 s57, 0x10000
	s_movk_i32 s56, 0x4000
	s_mov_b64 s[0:1], 0

; #define LAS __attribute__((address_space(3)))
; template <bool HAVE_PREV, bool HAVE_NEXT> __device__ __forceinline__ void sstep(f32x16& ca, f32x16& pa, const bf16x8 (&kf)[4], bf16x8 (&kn)[4], const LAS unsigned char* kbn, unsigned vpa, ...
;     const f32x16 z = {0.f, 0.f, 0.f, 0.f, 0.f, 0.f, 0.f, 0.f, 0.f, 0.f, 0.f, 0.f, 0.f, 0.f, 0.f, 0.f};
;     s16x4 vl[2][2], vh[2][2]; u32x4 wa[2];
;     ca = __builtin_amdgcn_mfma_f32_32x32x16_bf16(kf[0], qr[0], z, 0, 0, 0);
;     float a0, a1, a2, a3, a4, a5, a6, a7;
;     if (HAVE_PREV) { a0 = fadd_s(pa[0], pa[1]); a1 = fadd_s(pa[2], pa[3]); a2 = fadd_s(pa[4], pa[5]); a3 = fadd_s(pa[6], pa[7]); a4 = fadd_s(pa[8], pa[9]); a5 = fadd_s(pa[10], pa[11]); a6 = fadd_s(pa[12], pa[13]); a7 = fadd_s(pa[14], pa[15]);
;         wa[0].x = cvtpk(pa[0], pa[1]); wa[0].y = cvtpk(pa[2], pa[3]); wa[0].z = cvtpk(pa[4], pa[5]); wa[0].w = cvtpk(pa[6], pa[7]); }
;     ATT_SB();
;     ca = __builtin_amdgcn_mfma_f32_32x32x16_bf16(kf[1], qr[1], ca, 0, 0, 0);
;     if (HAVE_PREV) {
;         ATT_TR(vl[0][0], vpa, 0); ATT_TR(vh[0][0], vpa, 512); ATT_TR(vl[1][0], vpa, 4096); ATT_TR(vh[1][0], vpa, 4096 + 512);
;         ATT_TR(vl[0][1], vpa, 1024); ATT_TR(vh[0][1], vpa, 1024 + 512); ATT_TR(vl[1][1], vpa, 4096 + 1024); ATT_TR(vh[1][1], vpa, 4096 + 1024 + 512);
;         a0 = fadd_s(a0, a1); a2 = fadd_s(a2, a3); a4 = fadd_s(a4, a5); a6 = fadd_s(a6, a7);
;         wa[1].x = cvtpk(pa[8], pa[9]); wa[1].y = cvtpk(pa[10], pa[11]); wa[1].z = cvtpk(pa[12], pa[13]); wa[1].w = cvtpk(pa[14], pa[15]); }
;     ATT_SB();
;     ca = __builtin_amdgcn_mfma_f32_32x32x16_bf16(kf[2], qr[2], ca, 0, 0, 0);
;     if (HAVE_PREV) { a0 = fadd_s(a0, a2); a4 = fadd_s(a4, a6); }
;     ATT_SB();
; __device__ __forceinline__ void unit_swa(const P& p, LAS unsigned char* lds, const Src& S, const int qa  , const float sinkp, bf16_t* orow, const int wid,
;                                          bf16x8 (&qr)[4], const bool pre, const bool pn, const Src& Sn) {
;     ...
;     ATT_WAITV(0); ATT_BAR(); ATT_DMA(2, 2 * SLOTB); ATT_DMA(3, 3 * SLOTB);
; #pragma unroll
;     for (int d0 = 0; d0 < 4; ++d0) kA[d0] = *(const LAS bf16x8*)(lds + koff + d0 * 2048);
;     sstep<false, true>(A0, A1, kA, kB, lds + koff + 512, 0u, qr, o1, l1, SW_FULL(0, 0), SW_DQ(0, 0));
;     sstep<true, true>(A1, A0, kB, kA, lds + SLOTB + koff, lbase + voff, qr, o1, l1, SW_FULL(0, 1), SW_DQ(0, 1));
.LBB7_489:
	s_add_i32 s6, s44, 2
	s_lshl_b32 s58, s44, 6
	s_lshl_b64 s[46:47], s[6:7], 13
	s_add_u32 s6, s1, s46
	s_addc_u32 s45, s11, s47
	s_add_u32 s55, s36, s46
	s_addc_u32 s56, s37, s47
	s_cmp_gt_i32 s51, 1
	s_cselect_b32 s47, s45, s48
	s_cselect_b32 s46, s6, s38
	s_cselect_b32 s57, s56, s50
	s_cselect_b32 s56, s55, s49
	v_lshlrev_b64 v[106:107], 1, v[0:1]
	s_add_i32 s6, s44, 3
	v_lshl_add_u64 v[0:1], s[46:47], 0, v[106:107]
	s_lshl_b64 s[46:47], s[6:7], 13
	s_add_u32 s6, s1, s46
	s_waitcnt vmcnt(0)
	s_addc_u32 s45, s11, s47
	s_mov_b32 m0, s85
	s_waitcnt lgkmcnt(0)
	s_barrier
	s_add_u32 s55, s36, s46
	global_load_lds_dwordx4 v[0:1], off
	v_lshl_add_u64 v[0:1], s[56:57], 0, v[106:107]
	s_addc_u32 s56, s37, s47
	s_cmp_gt_i32 s51, 2
	s_mov_b32 m0, s87
	s_cselect_b32 s47, s45, s48
	s_cselect_b32 s46, s6, s38
	global_load_lds_dwordx4 v[0:1], off
	s_cselect_b32 s57, s56, s50
	s_cselect_b32 s56, s55, s49
	v_lshl_add_u64 v[0:1], s[46:47], 0, v[106:107]
	s_mov_b32 m0, s88
	s_or_b32 s45, s9, 31
	global_load_lds_dwordx4 v[0:1], off
	v_lshl_add_u64 v[0:1], s[56:57], 0, v[106:107]
	s_mov_b32 m0, s90
	s_sub_i32 s6, s58, s9
	global_load_lds_dwordx4 v[0:1], off
	v_lshlrev_b32_e32 v0, 4, v110
	v_lshl_or_b32 v0, v109, 10, v0
	v_add_u32_e32 v114, 0, v0
	ds_read_b128 v[0:3], v114
	ds_read_b128 v[16:19], v114 offset:2048
	ds_read_b128 v[20:23], v114 offset:4096
	ds_read_b128 v[24:27], v114 offset:6144
	s_waitcnt vmcnt(4) lgkmcnt(0)
	v_mfma_f32_32x32x16_bf16 v[0:15], v[0:3], v[64:67], 0
	s_sub_i32 s46, s45, s58
	s_or_b32 s47, s6, 31
	v_lshlrev_b32_e32 v112, 2, v109
	s_max_i32 s46, s46, s47
	v_or_b32_e32 v96, s9, v110
	s_cmpk_lt_i32 s46, 0x81
	v_mfma_f32_32x32x16_bf16 v[0:15], v[16:19], v[68:71], v[0:15]
	v_mfma_f32_32x32x16_bf16 v[0:15], v[20:23], v[72:75], v[0:15]
	v_mfma_f32_32x32x16_bf16 v[0:15], v[24:27], v[76:79], v[0:15]
	s_waitcnt lgkmcnt(0)
	ds_read_b128 v[28:31], v114 offset:512
	ds_read_b128 v[24:27], v114 offset:2560
	ds_read_b128 v[20:23], v114 offset:4608
	ds_read_b128 v[16:19], v114 offset:6656
	s_cbranch_scc1 .LBB7_491
	v_add_u32_e32 v32, s58, v112
	v_sub_u32_e32 v32, v96, v32
	v_add_u32_e32 v33, 0xffffff7f, v32
	v_cmp_lt_u32_e32 vcc, s91, v33
	v_add_u32_e32 v33, 0xffffff7e, v32
	s_nop 1
	v_cndmask_b32_e32 v0, v155, v0, vcc
	v_cmp_lt_u32_e32 vcc, s91, v33
	v_add_u32_e32 v33, 0xffffff7d, v32
	s_nop 0
	v_cndmask_b32_e32 v1, v155, v1, vcc
	v_cmp_lt_u32_e32 vcc, s91, v33
	v_add_u32_e32 v33, 0xffffff7c, v32
	s_nop 0
	v_cndmask_b32_e32 v2, v155, v2, vcc
	v_cmp_lt_u32_e32 vcc, s91, v33
	v_add_u32_e32 v33, 0xffffff77, v32
	s_nop 0
	v_cndmask_b32_e32 v3, v155, v3, vcc
	v_cmp_lt_u32_e32 vcc, s91, v33
	v_add_u32_e32 v33, 0xffffff76, v32
	s_nop 0
	v_cndmask_b32_e32 v4, v155, v4, vcc
	v_cmp_lt_u32_e32 vcc, s91, v33
	v_add_u32_e32 v33, 0xffffff75, v32
	s_nop 0
	v_cndmask_b32_e32 v5, v155, v5, vcc
	v_cmp_lt_u32_e32 vcc, s91, v33
	v_add_u32_e32 v33, 0xffffff74, v32
	s_nop 0
	v_cndmask_b32_e32 v6, v155, v6, vcc
	v_cmp_lt_u32_e32 vcc, s91, v33
	v_add_u32_e32 v33, 0xffffff6f, v32
	s_nop 0
	v_cndmask_b32_e32 v7, v155, v7, vcc
	v_cmp_lt_u32_e32 vcc, s91, v33
	v_add_u32_e32 v33, 0xffffff6e, v32
	s_nop 0
	v_cndmask_b32_e32 v8, v155, v8, vcc
	v_cmp_lt_u32_e32 vcc, s91, v33
	v_add_u32_e32 v33, 0xffffff6d, v32
	s_nop 0
	v_cndmask_b32_e32 v9, v155, v9, vcc
	v_cmp_lt_u32_e32 vcc, s91, v33
	v_add_u32_e32 v33, 0xffffff6c, v32
	s_nop 0
	v_cndmask_b32_e32 v10, v155, v10, vcc
	v_cmp_lt_u32_e32 vcc, s91, v33
	v_add_u32_e32 v33, 0xffffff67, v32
	s_nop 0
	v_cndmask_b32_e32 v11, v155, v11, vcc
	v_cmp_lt_u32_e32 vcc, s91, v33
	v_add_u32_e32 v33, 0xffffff66, v32
	s_nop 0
	v_cndmask_b32_e32 v12, v155, v12, vcc
	v_cmp_lt_u32_e32 vcc, s91, v33
	v_add_u32_e32 v33, 0xffffff65, v32
	v_add_u32_e32 v32, 0xffffff64, v32
	v_cndmask_b32_e32 v13, v155, v13, vcc
	v_cmp_lt_u32_e32 vcc, s91, v33
	s_nop 1
	v_cndmask_b32_e32 v14, v155, v14, vcc
	v_cmp_lt_u32_e32 vcc, s91, v32
	s_nop 1
	v_cndmask_b32_e32 v15, v155, v15, vcc
